# attention main loop: cross-half row-max combine (mov, nop, permlane swap, max) moved into the rare rescale block; rescale path checked with a THR=0 build
# speedup vs baseline: 1.0165x; 1.0016x over previous
.LBB0_1028:
	v_add_u32_e32 v230, s44, v228
	ds_read_b64_tr_b16 v[190:191], v230 offset:49152
	ds_read_b64_tr_b16 v[192:193], v230 offset:49664
	s_waitcnt lgkmcnt(9)
	v_mfma_f32_32x32x16_bf16 v[114:129], v[102:105], v[158:161], v[236:251]
	v_add_f32_e32 v106, v82, v83
	v_add_f32_e32 v106, v84, v106
	v_add_f32_e32 v106, v85, v106
	v_add_f32_e32 v106, v86, v106
	v_add_f32_e32 v106, v87, v106
	v_cvt_pk_bf16_f32 v150, v82, v83
	v_cvt_pk_bf16_f32 v151, v84, v85
	ds_read_b64_tr_b16 v[186:187], v230 offset:53248
	ds_read_b64_tr_b16 v[188:189], v230 offset:53760
	v_add_f32_e32 v82, v88, v106
	s_waitcnt lgkmcnt(10)
	v_mfma_f32_32x32x16_bf16 v[98:113], v[98:101], v[158:161], v[236:251]
	v_add_f32_e32 v82, v89, v82
	v_add_f32_e32 v82, v90, v82
	v_add_f32_e32 v130, v91, v82
	v_cvt_pk_bf16_f32 v152, v86, v87
	v_cvt_pk_bf16_f32 v153, v88, v89
	ds_read_b64_tr_b16 v[82:83], v230 offset:57344
	ds_read_b64_tr_b16 v[84:85], v230 offset:57856
	s_waitcnt lgkmcnt(11)
	v_mfma_f32_32x32x16_bf16 v[114:129], v[182:185], v[154:157], v[114:129]
	v_add_f32_e32 v86, v92, v130
	v_add_f32_e32 v86, v93, v86
	v_add_f32_e32 v86, v94, v86
	v_add_f32_e32 v130, v95, v86
	v_cvt_pk_bf16_f32 v138, v90, v91
	v_cvt_pk_bf16_f32 v139, v92, v93
	ds_read_b64_tr_b16 v[86:87], v230 offset:61440
	ds_read_b64_tr_b16 v[88:89], v230 offset:61952
	s_waitcnt lgkmcnt(12)
	v_mfma_f32_32x32x16_bf16 v[98:113], v[178:181], v[154:157], v[98:113]
	v_add_f32_e32 v90, v96, v130
	v_add_f32_e32 v90, v97, v90
	v_add_f32_e32 v90, v66, v90
	v_add_f32_e32 v130, v67, v90
	v_cvt_pk_bf16_f32 v140, v94, v95
	v_cvt_pk_bf16_f32 v141, v96, v97
	ds_read_b64_tr_b16 v[90:91], v230 offset:50176
	ds_read_b64_tr_b16 v[92:93], v230 offset:50688
	s_waitcnt lgkmcnt(13)
	v_mfma_f32_32x32x16_bf16 v[114:129], v[174:177], v[146:149], v[114:129]
	v_add_f32_e32 v94, v68, v130
	v_add_f32_e32 v94, v69, v94
	v_add_f32_e32 v94, v70, v94
	v_add_f32_e32 v130, v71, v94
	v_cvt_pk_bf16_f32 v134, v66, v67
	v_cvt_pk_bf16_f32 v135, v68, v69
	ds_read_b64_tr_b16 v[94:95], v230 offset:54272
	ds_read_b64_tr_b16 v[96:97], v230 offset:54784
	s_waitcnt lgkmcnt(14)
	v_mfma_f32_32x32x16_bf16 v[98:113], v[170:173], v[146:149], v[98:113]
	v_add_f32_e32 v66, v72, v130
	v_add_f32_e32 v66, v73, v66
	v_add_f32_e32 v66, v74, v66
	v_add_f32_e32 v66, v75, v66
	v_cvt_pk_bf16_f32 v136, v70, v71
	v_cvt_pk_bf16_f32 v137, v72, v73
	ds_read_b64_tr_b16 v[194:195], v230 offset:58368
	ds_read_b64_tr_b16 v[196:197], v230 offset:58880
	s_waitcnt lgkmcnt(14)
	v_mfma_f32_32x32x16_bf16 v[114:129], v[166:169], v[142:145], v[114:129]
	v_add_f32_e32 v66, v76, v66
	v_add_f32_e32 v66, v77, v66
	v_add_f32_e32 v66, v78, v66
	v_add_f32_e32 v66, v79, v66
	v_cvt_pk_bf16_f32 v130, v74, v75
	v_cvt_pk_bf16_f32 v131, v76, v77
	ds_read_b64_tr_b16 v[74:75], v230 offset:62464
	ds_read_b64_tr_b16 v[76:77], v230 offset:62976
	v_mfma_f32_32x32x16_bf16 v[98:113], v[162:165], v[142:145], v[98:113]
	v_add_f32_e32 v66, v80, v66
	v_add_f32_e32 v66, v81, v66
	v_cvt_pk_bf16_f32 v132, v78, v79
	v_cvt_pk_bf16_f32 v133, v80, v81
	s_add_i32 s4, s10, s89
	s_mov_b32 s5, m0
	s_mov_b32 m0, s4
	s_nop 0
	global_load_lds_dwordx4 v[220:221], off
	s_mov_b32 m0, s5
	v_add_f32_e32 v234, v234, v66
	s_addk_i32 s4, 0x400
	s_mov_b32 s5, m0
	s_mov_b32 m0, s4
	s_nop 0
	global_load_lds_dwordx4 v[218:219], off
	s_mov_b32 m0, s5
	v_lshl_add_u64 v[66:67], v[224:225], 0, s[0:1]
	s_add_i32 s4, s9, s70
	s_mov_b32 s5, m0
	s_mov_b32 m0, s4
	s_nop 0
	global_load_lds_dwordx4 v[66:67], off
	s_mov_b32 m0, s5
	v_lshl_add_u64 v[66:67], v[224:225], 0, s[64:65]
	s_addk_i32 s4, 0x400
	s_mov_b32 s5, m0
	s_mov_b32 m0, s4
	s_nop 0
	global_load_lds_dwordx4 v[66:67], off
	s_mov_b32 m0, s5
	v_max_f32_e32 v66, v114, v115
	v_max3_f32 v67, v116, v117, v99
	v_max3_f32 v66, v66, v98, v100
	v_max3_f32 v66, v66, v101, v118
	v_max3_f32 v67, v67, v120, v121
	v_max3_f32 v66, v66, v119, v102
	v_max3_f32 v67, v67, v104, v105
	v_max3_f32 v66, v66, v103, v122
	v_max3_f32 v67, v67, v124, v125
	v_max3_f32 v66, v66, v123, v106
	v_max3_f32 v67, v67, v108, v109
	v_max3_f32 v66, v66, v107, v126
	v_max3_f32 v67, v67, v128, v129
	v_max3_f32 v66, v66, v127, v110
	v_max3_f32 v67, v67, v112, v113
	v_max3_f32 v66, v66, v111, v67
	s_mov_b64 s[4:5], 0
	v_cmp_lt_f32_e32 vcc, s3, v66
	s_cbranch_vccnz .LBB0_1036

.LBB0_1031:
	s_add_i32 s4, s9, 0x4000
	s_cmpk_lg_u32 s9, 0x8000
	s_cselect_b32 s11, s4, 0
	v_add_u32_e32 v230, s10, v228
	ds_read_b64_tr_b16 v[190:191], v230 offset:49152
	ds_read_b64_tr_b16 v[192:193], v230 offset:49664
	v_mfma_f32_32x32x16_bf16 v[82:97], v[70:73], v[158:161], v[236:251]
	v_add_f32_e32 v74, v114, v115
	v_add_f32_e32 v74, v116, v74
	v_add_f32_e32 v74, v117, v74
	v_add_f32_e32 v74, v118, v74
	v_add_f32_e32 v74, v119, v74
	v_cvt_pk_bf16_f32 v150, v114, v115
	v_cvt_pk_bf16_f32 v151, v116, v117
	ds_read_b64_tr_b16 v[186:187], v230 offset:53248
	ds_read_b64_tr_b16 v[188:189], v230 offset:53760
	v_add_f32_e32 v70, v120, v74
	v_add_f32_e32 v70, v121, v70
	v_add_f32_e32 v70, v122, v70
	v_add_f32_e32 v130, v123, v70
	v_mfma_f32_32x32x16_bf16 v[66:81], v[66:69], v[158:161], v[236:251]
	v_cvt_pk_bf16_f32 v152, v118, v119
	v_cvt_pk_bf16_f32 v153, v120, v121
	ds_read_b64_tr_b16 v[114:115], v230 offset:57344
	ds_read_b64_tr_b16 v[116:117], v230 offset:57856
	v_mfma_f32_32x32x16_bf16 v[82:97], v[182:185], v[154:157], v[82:97]
	v_add_f32_e32 v118, v124, v130
	v_add_f32_e32 v118, v125, v118
	v_add_f32_e32 v118, v126, v118
	v_add_f32_e32 v130, v127, v118
	v_cvt_pk_bf16_f32 v138, v122, v123
	v_cvt_pk_bf16_f32 v139, v124, v125
	ds_read_b64_tr_b16 v[118:119], v230 offset:61440
	ds_read_b64_tr_b16 v[120:121], v230 offset:61952
	v_mfma_f32_32x32x16_bf16 v[66:81], v[178:181], v[154:157], v[66:81]
	v_add_f32_e32 v122, v128, v130
	v_add_f32_e32 v122, v129, v122
	v_add_f32_e32 v122, v98, v122
	v_add_f32_e32 v130, v99, v122
	v_cvt_pk_bf16_f32 v140, v126, v127
	v_cvt_pk_bf16_f32 v141, v128, v129
	ds_read_b64_tr_b16 v[122:123], v230 offset:50176
	ds_read_b64_tr_b16 v[124:125], v230 offset:50688
	v_mfma_f32_32x32x16_bf16 v[82:97], v[174:177], v[146:149], v[82:97]
	v_add_f32_e32 v126, v100, v130
	v_add_f32_e32 v126, v101, v126
	v_add_f32_e32 v126, v102, v126
	v_add_f32_e32 v130, v103, v126
	v_cvt_pk_bf16_f32 v134, v98, v99
	v_cvt_pk_bf16_f32 v135, v100, v101
	ds_read_b64_tr_b16 v[126:127], v230 offset:54272
	ds_read_b64_tr_b16 v[128:129], v230 offset:54784
	v_mfma_f32_32x32x16_bf16 v[66:81], v[170:173], v[146:149], v[66:81]
	v_add_f32_e32 v98, v104, v130
	v_add_f32_e32 v98, v105, v98
	v_add_f32_e32 v98, v106, v98
	v_add_f32_e32 v98, v107, v98
	v_cvt_pk_bf16_f32 v136, v102, v103
	v_cvt_pk_bf16_f32 v137, v104, v105
	ds_read_b64_tr_b16 v[194:195], v230 offset:58368
	ds_read_b64_tr_b16 v[196:197], v230 offset:58880
	v_mfma_f32_32x32x16_bf16 v[82:97], v[166:169], v[142:145], v[82:97]
	v_add_f32_e32 v98, v108, v98
	v_add_f32_e32 v98, v109, v98
	v_add_f32_e32 v98, v110, v98
	v_add_f32_e32 v98, v111, v98
	v_cvt_pk_bf16_f32 v130, v106, v107
	v_cvt_pk_bf16_f32 v131, v108, v109
	ds_read_b64_tr_b16 v[106:107], v230 offset:62464
	ds_read_b64_tr_b16 v[108:109], v230 offset:62976
	v_mfma_f32_32x32x16_bf16 v[66:81], v[162:165], v[142:145], v[66:81]
	v_add_f32_e32 v98, v112, v98
	v_add_f32_e32 v98, v113, v98
	v_cvt_pk_bf16_f32 v132, v110, v111
	v_cvt_pk_bf16_f32 v133, v112, v113
	s_nop 0
	v_add_f32_e32 v234, v234, v98
	s_add_i32 s4, s9, s89
	v_lshl_add_u64 v[98:99], v[220:221], 0, s[0:1]
	s_mov_b32 s5, m0
	s_mov_b32 m0, s4
	s_nop 0
	global_load_lds_dwordx4 v[98:99], off
	s_mov_b32 m0, s5
	v_lshl_add_u64 v[98:99], v[218:219], 0, s[0:1]
	s_addk_i32 s4, 0x400
	s_mov_b32 s5, m0
	s_mov_b32 m0, s4
	s_nop 0
	global_load_lds_dwordx4 v[98:99], off
	s_mov_b32 m0, s5
	v_lshl_add_u64 v[110:111], v[224:225], 0, s[74:75]
	s_add_i32 s4, s11, s70
	s_mov_b32 s5, m0
	s_mov_b32 m0, s4
	s_nop 0
	global_load_lds_dwordx4 v[110:111], off
	s_mov_b32 m0, s5
	v_lshl_add_u64 v[98:99], v[224:225], 0, s[62:63]
	s_addk_i32 s4, 0x400
	s_mov_b32 s5, m0
	s_mov_b32 m0, s4
	s_nop 0
	global_load_lds_dwordx4 v[98:99], off
	s_mov_b32 m0, s5
	v_max_f32_e32 v98, v82, v83
	v_max3_f32 v99, v84, v85, v67
	v_max3_f32 v98, v98, v66, v68
	v_max3_f32 v98, v98, v69, v86
	v_max3_f32 v99, v99, v88, v89
	v_max3_f32 v98, v98, v87, v70
	v_max3_f32 v99, v99, v72, v73
	v_max3_f32 v98, v98, v71, v90
	v_max3_f32 v99, v99, v92, v93
	v_max3_f32 v98, v98, v91, v74
	v_max3_f32 v99, v99, v76, v77
	v_max3_f32 v98, v98, v75, v94
	v_max3_f32 v99, v99, v96, v97
	v_max3_f32 v98, v98, v95, v78
	v_max3_f32 v99, v99, v80, v81
	v_max3_f32 v98, v98, v79, v99
	s_mov_b64 s[4:5], 0
	v_cmp_lt_f32_e32 vcc, s3, v98
	s_cbranch_vccnz .LBB0_1039

.LBB0_1036:
	v_mov_b32_e32 v67, v66
	s_nop 1
	v_permlane32_swap_b32_e32 v66, v67
	v_max_f32_e32 v66, v66, v67
	v_max_f32_e32 v66, v66, v66
	v_max_f32_e32 v67, 0, v66
	v_exp_f32_e64 v66, -v67
	s_mov_b64 s[4:5], -1
	s_and_saveexec_b64 s[6:7], s[40:41]
	ds_write_b32 v205, v66
	s_or_b64 exec, exec, s[6:7]
	v_sub_f32_e32 v98, v98, v67
	v_sub_f32_e32 v99, v99, v67
	v_sub_f32_e32 v100, v100, v67
	v_sub_f32_e32 v101, v101, v67
	v_sub_f32_e32 v102, v102, v67
	v_sub_f32_e32 v103, v103, v67
	v_sub_f32_e32 v104, v104, v67
	v_sub_f32_e32 v105, v105, v67
	v_sub_f32_e32 v106, v106, v67
	v_sub_f32_e32 v107, v107, v67
	v_sub_f32_e32 v108, v108, v67
	v_sub_f32_e32 v109, v109, v67
	v_sub_f32_e32 v110, v110, v67
	v_sub_f32_e32 v111, v111, v67
	v_sub_f32_e32 v112, v112, v67
	v_sub_f32_e32 v113, v113, v67
	v_sub_f32_e32 v114, v114, v67
	v_sub_f32_e32 v115, v115, v67
	v_sub_f32_e32 v116, v116, v67
	v_sub_f32_e32 v117, v117, v67
	v_sub_f32_e32 v118, v118, v67
	v_sub_f32_e32 v119, v119, v67
	v_sub_f32_e32 v120, v120, v67
	v_sub_f32_e32 v121, v121, v67
	v_sub_f32_e32 v122, v122, v67
	v_sub_f32_e32 v123, v123, v67
	v_sub_f32_e32 v124, v124, v67
	v_sub_f32_e32 v125, v125, v67
	v_sub_f32_e32 v126, v126, v67
	v_sub_f32_e32 v127, v127, v67
	v_sub_f32_e32 v128, v128, v67
	v_sub_f32_e32 v129, v129, v67
	v_add_f32_e32 v207, v207, v67
	v_sub_f32_e32 v236, 0, v207
	v_sub_f32_e32 v237, 0, v207
	v_sub_f32_e32 v238, 0, v207
	v_sub_f32_e32 v239, 0, v207
	v_sub_f32_e32 v240, 0, v207
	v_sub_f32_e32 v241, 0, v207
	v_sub_f32_e32 v242, 0, v207
	v_sub_f32_e32 v243, 0, v207
	v_sub_f32_e32 v244, 0, v207
	v_sub_f32_e32 v245, 0, v207
	v_sub_f32_e32 v246, 0, v207
	v_sub_f32_e32 v247, 0, v207
	v_sub_f32_e32 v248, 0, v207
	v_sub_f32_e32 v249, 0, v207
	v_sub_f32_e32 v250, 0, v207
	v_sub_f32_e32 v251, 0, v207
	v_mul_f32_e32 v234, v234, v66
	s_branch .LBB0_1029
.LBB0_1039:
	v_mov_b32_e32 v99, v98
	s_nop 1
	v_permlane32_swap_b32_e32 v98, v99
	v_max_f32_e32 v98, v98, v99
	v_max_f32_e32 v98, v98, v98
	v_max_f32_e32 v99, 0, v98
	v_exp_f32_e64 v98, -v99
	s_mov_b64 s[4:5], -1
	s_and_saveexec_b64 s[6:7], s[40:41]
	ds_write_b32 v205, v98
	s_or_b64 exec, exec, s[6:7]
	v_sub_f32_e32 v66, v66, v99
	v_sub_f32_e32 v67, v67, v99
	v_sub_f32_e32 v68, v68, v99
	v_sub_f32_e32 v69, v69, v99
	v_sub_f32_e32 v70, v70, v99
	v_sub_f32_e32 v71, v71, v99
	v_sub_f32_e32 v72, v72, v99
	v_sub_f32_e32 v73, v73, v99
	v_sub_f32_e32 v74, v74, v99
	v_sub_f32_e32 v75, v75, v99
	v_sub_f32_e32 v76, v76, v99
	v_sub_f32_e32 v77, v77, v99
	v_sub_f32_e32 v78, v78, v99
	v_sub_f32_e32 v79, v79, v99
	v_sub_f32_e32 v80, v80, v99
	v_sub_f32_e32 v81, v81, v99
	v_sub_f32_e32 v82, v82, v99
	v_sub_f32_e32 v83, v83, v99
	v_sub_f32_e32 v84, v84, v99
	v_sub_f32_e32 v85, v85, v99
	v_sub_f32_e32 v86, v86, v99
	v_sub_f32_e32 v87, v87, v99
	v_sub_f32_e32 v88, v88, v99
	v_sub_f32_e32 v89, v89, v99
	v_sub_f32_e32 v90, v90, v99
	v_sub_f32_e32 v91, v91, v99
	v_sub_f32_e32 v92, v92, v99
	v_sub_f32_e32 v93, v93, v99
	v_sub_f32_e32 v94, v94, v99
	v_sub_f32_e32 v95, v95, v99
	v_sub_f32_e32 v96, v96, v99
	v_sub_f32_e32 v97, v97, v99
	v_add_f32_e32 v207, v207, v99
	v_sub_f32_e32 v236, 0, v207
	v_sub_f32_e32 v237, 0, v207
	v_sub_f32_e32 v238, 0, v207
	v_sub_f32_e32 v239, 0, v207
	v_sub_f32_e32 v240, 0, v207
	v_sub_f32_e32 v241, 0, v207
	v_sub_f32_e32 v242, 0, v207
	v_sub_f32_e32 v243, 0, v207
	v_sub_f32_e32 v244, 0, v207
	v_sub_f32_e32 v245, 0, v207
	v_sub_f32_e32 v246, 0, v207
	v_sub_f32_e32 v247, 0, v207
	v_sub_f32_e32 v248, 0, v207
	v_sub_f32_e32 v249, 0, v207
	v_sub_f32_e32 v250, 0, v207
	v_sub_f32_e32 v251, 0, v207
	v_mul_f32_e32 v234, v234, v98
	s_branch .LBB0_1032
